# also the three items each workgroup converts inside P6 go through the pipelined routine (static list mode, item split recomputed in scalar code)
# speedup vs baseline: 1.0050x; 1.0050x over previous
.LBB0_848:
	s_cmpk_lg_i32 s70, 0x100
	s_cbranch_scc1 .Lcvc_orig
	s_and_b32 s19, s48, 0xff
	s_sub_u32 s20, 0x100, s19
	s_lshl_b32 s21, s19, 1
	s_add_u32 s6, s60, 0x900
	s_add_u32 s7, s6, 0x100
	s_add_u32 s44, s6, 0x200
	s_mov_b32 s45, 0xffff
	s_cmp_eq_u32 s19, 0
	s_cbranch_scc1 .Lcvc_go
	s_cmp_gt_u32 s21, s20
	s_cbranch_scc1 .Lcvc_go
	s_mul_i32 s22, s20, 3
	s_cmp_lt_u32 s60, s19
	s_cbranch_scc0 .Lcvc_light
	s_add_u32 s6, s60, 0x900
	s_add_u32 s6, s6, s22
	s_mov_b32 s7, 0xffff
	s_mov_b32 s44, 0xffff
	s_mov_b32 s45, 0xffff
	s_branch .Lcvc_go
.Lcvc_light:
	s_sub_u32 s23, s60, s19
	s_add_u32 s6, s23, 0x900
	s_add_u32 s7, s6, s20
	s_add_u32 s44, s7, s20
	s_mov_b32 s45, 0xffff
	s_cmp_lt_u32 s23, s21
	s_cbranch_scc0 .Lcvc_go
	s_add_u32 s45, s60, 0x900
	s_add_u32 s45, s45, s22
.Lcvc_go:
	v_readlane_b32 s34, v255, 33
	v_readlane_b32 s35, v255, 34
	v_readlane_b32 s36, v255, 37
	v_readlane_b32 s37, v255, 38
	v_readlane_b32 s38, v255, 41
	v_readlane_b32 s39, v255, 42
	s_mov_b32 s40, s90
	s_mov_b32 s41, s91
	s_mov_b32 s24, 0xc00
.Lcvc_entry:
	s_mov_b64 exec, -1
	v_readlane_b32 s26, v255, 4
	v_mbcnt_lo_u32_b32 v1, -1, 0
	v_mbcnt_hi_u32_b32 v1, -1, v1
	s_lshr_b32 s19, s26, 6
	s_lshr_b32 s20, s19, 2
	s_and_b32 s21, s19, 3
	s_lshl_b32 s25, s20, 19
	s_lshl_b32 s22, s21, 10
	s_add_u32 s25, s25, s22
	v_lshlrev_b32_e32 v130, 4, v1
	v_add_u32_e32 v131, 0x2000, v130
	v_add_u32_e32 v132, 0x4000, v130
	v_add_u32_e32 v133, 0x6000, v130
	v_add_u32_e32 v134, 0x8000, v130
	v_add_u32_e32 v135, 0xa000, v130
	v_add_u32_e32 v136, 0xc000, v130
	v_add_u32_e32 v137, 0xe000, v130
	v_and_b32_e32 v150, 15, v1
	s_lshl_b32 s22, s20, 3
	v_xor_b32_e32 v150, s22, v150
	v_lshlrev_b32_e32 v151, 9, v1
	s_lshl_b32 s22, s21, 15
	v_add_u32_e32 v151, s22, v151
	v_xor_b32_e32 v138, 0, v150
	v_lshl_add_u32 v138, v138, 3, v151
	v_xor_b32_e32 v139, 1, v150
	v_lshl_add_u32 v139, v139, 3, v151
	v_xor_b32_e32 v140, 2, v150
	v_lshl_add_u32 v140, v140, 3, v151
	v_xor_b32_e32 v141, 3, v150
	v_lshl_add_u32 v141, v141, 3, v151
	v_xor_b32_e32 v142, 4, v150
	v_lshl_add_u32 v142, v142, 3, v151
	v_xor_b32_e32 v143, 5, v150
	v_lshl_add_u32 v143, v143, 3, v151
	v_xor_b32_e32 v144, 6, v150
	v_lshl_add_u32 v144, v144, 3, v151
	v_xor_b32_e32 v145, 7, v150
	v_lshl_add_u32 v145, v145, 3, v151
	v_add_u32_e32 v152, s26, v1
	v_lshrrev_b32_e32 v153, 3, v152
	v_and_b32_e32 v154, 7, v152
	v_bfe_u32 v155, v152, 5, 4
	v_lshlrev_b32_e32 v156, 1, v154
	v_and_b32_e32 v157, 14, v155
	v_xor_b32_e32 v156, v156, v157
	v_lshlrev_b32_e32 v156, 3, v156
	v_lshl_add_u32 v146, v153, 7, v156
	v_add_u32_e32 v147, 0x10000, v146
	v_lshlrev_b32_e32 v148, 4, v154
	v_lshl_add_u32 v148, v153, 11, v148
	v_and_b32_e32 v157, 1, v155
	v_cmp_ne_u32_e64 s[30:31], 0, v157
	v_mov_b32_e32 v248, 0x42800000
	v_mov_b32_e32 v249, 0x42800000
	v_mov_b32_e32 v250, 0
	v_mov_b32_e32 v251, 1
	v_mov_b32_e32 v252, 0x20800
	s_waitcnt lgkmcnt(0)
	s_barrier
	s_cmp_ge_u32 s6, s24
	s_cbranch_scc1 .Lcvc_done
	s_lshr_b32 s19, s6, 10
	s_and_b32 s20, s6, 0x3ff
	s_cmp_eq_u32 s19, 0
	s_cselect_b32 s0, s34, s36
	s_cselect_b32 s1, s35, s37
	s_cmp_eq_u32 s19, 2
	s_cselect_b32 s0, s38, s0
	s_cselect_b32 s1, s39, s1
	s_lshr_b32 s21, s20, 5
	s_lshl_b32 s21, s21, 24
	s_bfe_u32 s22, s20, 0x40001
	s_lshl_b32 s22, s22, 20
	s_add_u32 s21, s21, s22
	s_and_b32 s22, s20, 1
	s_lshl_b32 s22, s22, 12
	s_add_u32 s21, s21, s22
	s_add_u32 s21, s21, s25
	s_add_u32 s0, s0, s21
	s_addc_u32 s1, s1, 0
	global_load_dwordx4 v[2:5], v130, s[0:1] nt
	global_load_dwordx4 v[6:9], v131, s[0:1] nt
	global_load_dwordx4 v[10:13], v132, s[0:1] nt
	global_load_dwordx4 v[14:17], v133, s[0:1] nt
	global_load_dwordx4 v[18:21], v134, s[0:1] nt
	global_load_dwordx4 v[22:25], v135, s[0:1] nt
	global_load_dwordx4 v[26:29], v136, s[0:1] nt
	global_load_dwordx4 v[30:33], v137, s[0:1] nt
	s_add_u32 s0, s0, 0x10000
	s_addc_u32 s1, s1, 0
	global_load_dwordx4 v[34:37], v130, s[0:1] nt
	global_load_dwordx4 v[38:41], v131, s[0:1] nt
	global_load_dwordx4 v[42:45], v132, s[0:1] nt
	global_load_dwordx4 v[46:49], v133, s[0:1] nt
	global_load_dwordx4 v[50:53], v134, s[0:1] nt
	global_load_dwordx4 v[54:57], v135, s[0:1] nt
	global_load_dwordx4 v[58:61], v136, s[0:1] nt
	global_load_dwordx4 v[62:65], v137, s[0:1] nt
	s_add_u32 s0, s0, 0x10000
	s_addc_u32 s1, s1, 0
	global_load_dwordx4 v[66:69], v130, s[0:1] nt
	global_load_dwordx4 v[70:73], v131, s[0:1] nt
	global_load_dwordx4 v[74:77], v132, s[0:1] nt
	global_load_dwordx4 v[78:81], v133, s[0:1] nt
	global_load_dwordx4 v[82:85], v134, s[0:1] nt
	global_load_dwordx4 v[86:89], v135, s[0:1] nt
	global_load_dwordx4 v[90:93], v136, s[0:1] nt
	global_load_dwordx4 v[94:97], v137, s[0:1] nt
	s_add_u32 s0, s0, 0x10000
	s_addc_u32 s1, s1, 0
	s_waitcnt vmcnt(16)
	v_pk_mul_f32 v[2:3], v[2:3], v[248:249]
	v_pk_mul_f32 v[4:5], v[4:5], v[248:249]
	v_pk_mul_f32 v[6:7], v[6:7], v[248:249]
	v_pk_mul_f32 v[8:9], v[8:9], v[248:249]
	v_pk_mul_f32 v[10:11], v[10:11], v[248:249]
	v_pk_mul_f32 v[12:13], v[12:13], v[248:249]
	v_pk_mul_f32 v[14:15], v[14:15], v[248:249]
	v_pk_mul_f32 v[16:17], v[16:17], v[248:249]
	v_pk_mul_f32 v[18:19], v[18:19], v[248:249]
	v_pk_mul_f32 v[20:21], v[20:21], v[248:249]
	v_pk_mul_f32 v[22:23], v[22:23], v[248:249]
	v_pk_mul_f32 v[24:25], v[24:25], v[248:249]
	v_pk_mul_f32 v[26:27], v[26:27], v[248:249]
	v_pk_mul_f32 v[28:29], v[28:29], v[248:249]
	v_pk_mul_f32 v[30:31], v[30:31], v[248:249]
	v_pk_mul_f32 v[32:33], v[32:33], v[248:249]
	v_cvt_pk_fp8_f32 v200, v2, v6
	v_cvt_pk_fp8_f32 v201, v18, v22
	v_cvt_pk_fp8_f32 v202, v3, v7
	v_cvt_pk_fp8_f32 v203, v19, v23
	v_cvt_pk_fp8_f32 v204, v4, v8
	v_cvt_pk_fp8_f32 v205, v20, v24
	v_cvt_pk_fp8_f32 v206, v5, v9
	v_cvt_pk_fp8_f32 v207, v21, v25
	v_cvt_pk_fp8_f32 v200, v10, v14 op_sel:[0,0,1]
	v_cvt_pk_fp8_f32 v201, v26, v30 op_sel:[0,0,1]
	v_cvt_pk_fp8_f32 v202, v11, v15 op_sel:[0,0,1]
	v_cvt_pk_fp8_f32 v203, v27, v31 op_sel:[0,0,1]
	v_cvt_pk_fp8_f32 v204, v12, v16 op_sel:[0,0,1]
	v_cvt_pk_fp8_f32 v205, v28, v32 op_sel:[0,0,1]
	v_cvt_pk_fp8_f32 v206, v13, v17 op_sel:[0,0,1]
	v_cvt_pk_fp8_f32 v207, v29, v33 op_sel:[0,0,1]
	s_nop 0
	ds_write2_b64 v138, v[200:201], v[202:203] offset1:16
	ds_write2_b64 v138, v[204:205], v[206:207] offset0:32 offset1:48
	global_load_dwordx4 v[98:101], v130, s[0:1] nt
	global_load_dwordx4 v[102:105], v131, s[0:1] nt
	global_load_dwordx4 v[106:109], v132, s[0:1] nt
	global_load_dwordx4 v[110:113], v133, s[0:1] nt
	global_load_dwordx4 v[114:117], v134, s[0:1] nt
	global_load_dwordx4 v[118:121], v135, s[0:1] nt
	global_load_dwordx4 v[122:125], v136, s[0:1] nt
	global_load_dwordx4 v[126:129], v137, s[0:1] nt
	s_add_u32 s0, s0, 0x10000
	s_addc_u32 s1, s1, 0
	s_waitcnt vmcnt(16)
	v_pk_mul_f32 v[34:35], v[34:35], v[248:249]
	v_pk_mul_f32 v[36:37], v[36:37], v[248:249]
	v_pk_mul_f32 v[38:39], v[38:39], v[248:249]
	v_pk_mul_f32 v[40:41], v[40:41], v[248:249]
	v_pk_mul_f32 v[42:43], v[42:43], v[248:249]
	v_pk_mul_f32 v[44:45], v[44:45], v[248:249]
	v_pk_mul_f32 v[46:47], v[46:47], v[248:249]
	v_pk_mul_f32 v[48:49], v[48:49], v[248:249]
	v_pk_mul_f32 v[50:51], v[50:51], v[248:249]
	v_pk_mul_f32 v[52:53], v[52:53], v[248:249]
	v_pk_mul_f32 v[54:55], v[54:55], v[248:249]
	v_pk_mul_f32 v[56:57], v[56:57], v[248:249]
	v_pk_mul_f32 v[58:59], v[58:59], v[248:249]
	v_pk_mul_f32 v[60:61], v[60:61], v[248:249]
	v_pk_mul_f32 v[62:63], v[62:63], v[248:249]
	v_pk_mul_f32 v[64:65], v[64:65], v[248:249]
	v_cvt_pk_fp8_f32 v208, v34, v38
	v_cvt_pk_fp8_f32 v209, v50, v54
	v_cvt_pk_fp8_f32 v210, v35, v39
	v_cvt_pk_fp8_f32 v211, v51, v55
	v_cvt_pk_fp8_f32 v212, v36, v40
	v_cvt_pk_fp8_f32 v213, v52, v56
	v_cvt_pk_fp8_f32 v214, v37, v41
	v_cvt_pk_fp8_f32 v215, v53, v57
	v_cvt_pk_fp8_f32 v208, v42, v46 op_sel:[0,0,1]
	v_cvt_pk_fp8_f32 v209, v58, v62 op_sel:[0,0,1]
	v_cvt_pk_fp8_f32 v210, v43, v47 op_sel:[0,0,1]
	v_cvt_pk_fp8_f32 v211, v59, v63 op_sel:[0,0,1]
	v_cvt_pk_fp8_f32 v212, v44, v48 op_sel:[0,0,1]
	v_cvt_pk_fp8_f32 v213, v60, v64 op_sel:[0,0,1]
	v_cvt_pk_fp8_f32 v214, v45, v49 op_sel:[0,0,1]
	v_cvt_pk_fp8_f32 v215, v61, v65 op_sel:[0,0,1]
	s_nop 0
	ds_write2_b64 v139, v[208:209], v[210:211] offset1:16
	ds_write2_b64 v139, v[212:213], v[214:215] offset0:32 offset1:48
	global_load_dwordx4 v[2:5], v130, s[0:1] nt
	global_load_dwordx4 v[6:9], v131, s[0:1] nt
	global_load_dwordx4 v[10:13], v132, s[0:1] nt
	global_load_dwordx4 v[14:17], v133, s[0:1] nt
	global_load_dwordx4 v[18:21], v134, s[0:1] nt
	global_load_dwordx4 v[22:25], v135, s[0:1] nt
	global_load_dwordx4 v[26:29], v136, s[0:1] nt
	global_load_dwordx4 v[30:33], v137, s[0:1] nt
	s_add_u32 s0, s0, 0x10000
	s_addc_u32 s1, s1, 0
	s_waitcnt vmcnt(16)
	v_pk_mul_f32 v[66:67], v[66:67], v[248:249]
	v_pk_mul_f32 v[68:69], v[68:69], v[248:249]
	v_pk_mul_f32 v[70:71], v[70:71], v[248:249]
	v_pk_mul_f32 v[72:73], v[72:73], v[248:249]
	v_pk_mul_f32 v[74:75], v[74:75], v[248:249]
	v_pk_mul_f32 v[76:77], v[76:77], v[248:249]
	v_pk_mul_f32 v[78:79], v[78:79], v[248:249]
	v_pk_mul_f32 v[80:81], v[80:81], v[248:249]
	v_pk_mul_f32 v[82:83], v[82:83], v[248:249]
	v_pk_mul_f32 v[84:85], v[84:85], v[248:249]
	v_pk_mul_f32 v[86:87], v[86:87], v[248:249]
	v_pk_mul_f32 v[88:89], v[88:89], v[248:249]
	v_pk_mul_f32 v[90:91], v[90:91], v[248:249]
	v_pk_mul_f32 v[92:93], v[92:93], v[248:249]
	v_pk_mul_f32 v[94:95], v[94:95], v[248:249]
	v_pk_mul_f32 v[96:97], v[96:97], v[248:249]
	v_cvt_pk_fp8_f32 v200, v66, v70
	v_cvt_pk_fp8_f32 v201, v82, v86
	v_cvt_pk_fp8_f32 v202, v67, v71
	v_cvt_pk_fp8_f32 v203, v83, v87
	v_cvt_pk_fp8_f32 v204, v68, v72
	v_cvt_pk_fp8_f32 v205, v84, v88
	v_cvt_pk_fp8_f32 v206, v69, v73
	v_cvt_pk_fp8_f32 v207, v85, v89
	v_cvt_pk_fp8_f32 v200, v74, v78 op_sel:[0,0,1]
	v_cvt_pk_fp8_f32 v201, v90, v94 op_sel:[0,0,1]
	v_cvt_pk_fp8_f32 v202, v75, v79 op_sel:[0,0,1]
	v_cvt_pk_fp8_f32 v203, v91, v95 op_sel:[0,0,1]
	v_cvt_pk_fp8_f32 v204, v76, v80 op_sel:[0,0,1]
	v_cvt_pk_fp8_f32 v205, v92, v96 op_sel:[0,0,1]
	v_cvt_pk_fp8_f32 v206, v77, v81 op_sel:[0,0,1]
	v_cvt_pk_fp8_f32 v207, v93, v97 op_sel:[0,0,1]
	s_nop 0
	ds_write2_b64 v140, v[200:201], v[202:203] offset1:16
	ds_write2_b64 v140, v[204:205], v[206:207] offset0:32 offset1:48
	global_load_dwordx4 v[34:37], v130, s[0:1] nt
	global_load_dwordx4 v[38:41], v131, s[0:1] nt
	global_load_dwordx4 v[42:45], v132, s[0:1] nt
	global_load_dwordx4 v[46:49], v133, s[0:1] nt
	global_load_dwordx4 v[50:53], v134, s[0:1] nt
	global_load_dwordx4 v[54:57], v135, s[0:1] nt
	global_load_dwordx4 v[58:61], v136, s[0:1] nt
	global_load_dwordx4 v[62:65], v137, s[0:1] nt
	s_add_u32 s0, s0, 0x10000
	s_addc_u32 s1, s1, 0
	s_branch .Lcvc_s3
.Lcvc_loop:
	s_waitcnt vmcnt(32)
	v_pk_mul_f32 v[2:3], v[2:3], v[248:249]
	v_pk_mul_f32 v[4:5], v[4:5], v[248:249]
	v_pk_mul_f32 v[6:7], v[6:7], v[248:249]
	v_pk_mul_f32 v[8:9], v[8:9], v[248:249]
	v_pk_mul_f32 v[10:11], v[10:11], v[248:249]
	v_pk_mul_f32 v[12:13], v[12:13], v[248:249]
	v_pk_mul_f32 v[14:15], v[14:15], v[248:249]
	v_pk_mul_f32 v[16:17], v[16:17], v[248:249]
	v_pk_mul_f32 v[18:19], v[18:19], v[248:249]
	v_pk_mul_f32 v[20:21], v[20:21], v[248:249]
	v_pk_mul_f32 v[22:23], v[22:23], v[248:249]
	v_pk_mul_f32 v[24:25], v[24:25], v[248:249]
	v_pk_mul_f32 v[26:27], v[26:27], v[248:249]
	v_pk_mul_f32 v[28:29], v[28:29], v[248:249]
	v_pk_mul_f32 v[30:31], v[30:31], v[248:249]
	v_pk_mul_f32 v[32:33], v[32:33], v[248:249]
	v_cvt_pk_fp8_f32 v200, v2, v6
	v_cvt_pk_fp8_f32 v201, v18, v22
	v_cvt_pk_fp8_f32 v202, v3, v7
	v_cvt_pk_fp8_f32 v203, v19, v23
	v_cvt_pk_fp8_f32 v204, v4, v8
	v_cvt_pk_fp8_f32 v205, v20, v24
	v_cvt_pk_fp8_f32 v206, v5, v9
	v_cvt_pk_fp8_f32 v207, v21, v25
	v_cvt_pk_fp8_f32 v200, v10, v14 op_sel:[0,0,1]
	v_cvt_pk_fp8_f32 v201, v26, v30 op_sel:[0,0,1]
	v_cvt_pk_fp8_f32 v202, v11, v15 op_sel:[0,0,1]
	v_cvt_pk_fp8_f32 v203, v27, v31 op_sel:[0,0,1]
	v_cvt_pk_fp8_f32 v204, v12, v16 op_sel:[0,0,1]
	v_cvt_pk_fp8_f32 v205, v28, v32 op_sel:[0,0,1]
	v_cvt_pk_fp8_f32 v206, v13, v17 op_sel:[0,0,1]
	v_cvt_pk_fp8_f32 v207, v29, v33 op_sel:[0,0,1]
	s_nop 0
	ds_write2_b64 v138, v[200:201], v[202:203] offset1:16
	ds_write2_b64 v138, v[204:205], v[206:207] offset0:32 offset1:48
	global_load_dwordx4 v[98:101], v130, s[0:1] nt
	global_load_dwordx4 v[102:105], v131, s[0:1] nt
	global_load_dwordx4 v[106:109], v132, s[0:1] nt
	global_load_dwordx4 v[110:113], v133, s[0:1] nt
	global_load_dwordx4 v[114:117], v134, s[0:1] nt
	global_load_dwordx4 v[118:121], v135, s[0:1] nt
	global_load_dwordx4 v[122:125], v136, s[0:1] nt
	global_load_dwordx4 v[126:129], v137, s[0:1] nt
	s_add_u32 s0, s0, 0x10000
	s_addc_u32 s1, s1, 0
	s_waitcnt vmcnt(32)
	v_pk_mul_f32 v[34:35], v[34:35], v[248:249]
	v_pk_mul_f32 v[36:37], v[36:37], v[248:249]
	v_pk_mul_f32 v[38:39], v[38:39], v[248:249]
	v_pk_mul_f32 v[40:41], v[40:41], v[248:249]
	v_pk_mul_f32 v[42:43], v[42:43], v[248:249]
	v_pk_mul_f32 v[44:45], v[44:45], v[248:249]
	v_pk_mul_f32 v[46:47], v[46:47], v[248:249]
	v_pk_mul_f32 v[48:49], v[48:49], v[248:249]
	v_pk_mul_f32 v[50:51], v[50:51], v[248:249]
	v_pk_mul_f32 v[52:53], v[52:53], v[248:249]
	v_pk_mul_f32 v[54:55], v[54:55], v[248:249]
	v_pk_mul_f32 v[56:57], v[56:57], v[248:249]
	v_pk_mul_f32 v[58:59], v[58:59], v[248:249]
	v_pk_mul_f32 v[60:61], v[60:61], v[248:249]
	v_pk_mul_f32 v[62:63], v[62:63], v[248:249]
	v_pk_mul_f32 v[64:65], v[64:65], v[248:249]
	v_cvt_pk_fp8_f32 v208, v34, v38
	v_cvt_pk_fp8_f32 v209, v50, v54
	v_cvt_pk_fp8_f32 v210, v35, v39
	v_cvt_pk_fp8_f32 v211, v51, v55
	v_cvt_pk_fp8_f32 v212, v36, v40
	v_cvt_pk_fp8_f32 v213, v52, v56
	v_cvt_pk_fp8_f32 v214, v37, v41
	v_cvt_pk_fp8_f32 v215, v53, v57
	v_cvt_pk_fp8_f32 v208, v42, v46 op_sel:[0,0,1]
	v_cvt_pk_fp8_f32 v209, v58, v62 op_sel:[0,0,1]
	v_cvt_pk_fp8_f32 v210, v43, v47 op_sel:[0,0,1]
	v_cvt_pk_fp8_f32 v211, v59, v63 op_sel:[0,0,1]
	v_cvt_pk_fp8_f32 v212, v44, v48 op_sel:[0,0,1]
	v_cvt_pk_fp8_f32 v213, v60, v64 op_sel:[0,0,1]
	v_cvt_pk_fp8_f32 v214, v45, v49 op_sel:[0,0,1]
	v_cvt_pk_fp8_f32 v215, v61, v65 op_sel:[0,0,1]
	s_nop 0
	ds_write2_b64 v139, v[208:209], v[210:211] offset1:16
	ds_write2_b64 v139, v[212:213], v[214:215] offset0:32 offset1:48
	global_load_dwordx4 v[2:5], v130, s[0:1] nt
	global_load_dwordx4 v[6:9], v131, s[0:1] nt
	global_load_dwordx4 v[10:13], v132, s[0:1] nt
	global_load_dwordx4 v[14:17], v133, s[0:1] nt
	global_load_dwordx4 v[18:21], v134, s[0:1] nt
	global_load_dwordx4 v[22:25], v135, s[0:1] nt
	global_load_dwordx4 v[26:29], v136, s[0:1] nt
	global_load_dwordx4 v[30:33], v137, s[0:1] nt
	s_add_u32 s0, s0, 0x10000
	s_addc_u32 s1, s1, 0
	s_waitcnt vmcnt(32)
	v_pk_mul_f32 v[66:67], v[66:67], v[248:249]
	v_pk_mul_f32 v[68:69], v[68:69], v[248:249]
	v_pk_mul_f32 v[70:71], v[70:71], v[248:249]
	v_pk_mul_f32 v[72:73], v[72:73], v[248:249]
	v_pk_mul_f32 v[74:75], v[74:75], v[248:249]
	v_pk_mul_f32 v[76:77], v[76:77], v[248:249]
	v_pk_mul_f32 v[78:79], v[78:79], v[248:249]
	v_pk_mul_f32 v[80:81], v[80:81], v[248:249]
	v_pk_mul_f32 v[82:83], v[82:83], v[248:249]
	v_pk_mul_f32 v[84:85], v[84:85], v[248:249]
	v_pk_mul_f32 v[86:87], v[86:87], v[248:249]
	v_pk_mul_f32 v[88:89], v[88:89], v[248:249]
	v_pk_mul_f32 v[90:91], v[90:91], v[248:249]
	v_pk_mul_f32 v[92:93], v[92:93], v[248:249]
	v_pk_mul_f32 v[94:95], v[94:95], v[248:249]
	v_pk_mul_f32 v[96:97], v[96:97], v[248:249]
	v_cvt_pk_fp8_f32 v200, v66, v70
	v_cvt_pk_fp8_f32 v201, v82, v86
	v_cvt_pk_fp8_f32 v202, v67, v71
	v_cvt_pk_fp8_f32 v203, v83, v87
	v_cvt_pk_fp8_f32 v204, v68, v72
	v_cvt_pk_fp8_f32 v205, v84, v88
	v_cvt_pk_fp8_f32 v206, v69, v73
	v_cvt_pk_fp8_f32 v207, v85, v89
	v_cvt_pk_fp8_f32 v200, v74, v78 op_sel:[0,0,1]
	v_cvt_pk_fp8_f32 v201, v90, v94 op_sel:[0,0,1]
	v_cvt_pk_fp8_f32 v202, v75, v79 op_sel:[0,0,1]
	v_cvt_pk_fp8_f32 v203, v91, v95 op_sel:[0,0,1]
	v_cvt_pk_fp8_f32 v204, v76, v80 op_sel:[0,0,1]
	v_cvt_pk_fp8_f32 v205, v92, v96 op_sel:[0,0,1]
	v_cvt_pk_fp8_f32 v206, v77, v81 op_sel:[0,0,1]
	v_cvt_pk_fp8_f32 v207, v93, v97 op_sel:[0,0,1]
	s_nop 0
	ds_write2_b64 v140, v[200:201], v[202:203] offset1:16
	ds_write2_b64 v140, v[204:205], v[206:207] offset0:32 offset1:48
	global_load_dwordx4 v[34:37], v130, s[0:1] nt
	global_load_dwordx4 v[38:41], v131, s[0:1] nt
	global_load_dwordx4 v[42:45], v132, s[0:1] nt
	global_load_dwordx4 v[46:49], v133, s[0:1] nt
	global_load_dwordx4 v[50:53], v134, s[0:1] nt
	global_load_dwordx4 v[54:57], v135, s[0:1] nt
	global_load_dwordx4 v[58:61], v136, s[0:1] nt
	global_load_dwordx4 v[62:65], v137, s[0:1] nt
	s_add_u32 s0, s0, 0x10000
	s_addc_u32 s1, s1, 0
.Lcvc_s3:
	s_waitcnt vmcnt(16)
	v_pk_mul_f32 v[98:99], v[98:99], v[248:249]
	v_pk_mul_f32 v[100:101], v[100:101], v[248:249]
	v_pk_mul_f32 v[102:103], v[102:103], v[248:249]
	v_pk_mul_f32 v[104:105], v[104:105], v[248:249]
	v_pk_mul_f32 v[106:107], v[106:107], v[248:249]
	v_pk_mul_f32 v[108:109], v[108:109], v[248:249]
	v_pk_mul_f32 v[110:111], v[110:111], v[248:249]
	v_pk_mul_f32 v[112:113], v[112:113], v[248:249]
	v_pk_mul_f32 v[114:115], v[114:115], v[248:249]
	v_pk_mul_f32 v[116:117], v[116:117], v[248:249]
	v_pk_mul_f32 v[118:119], v[118:119], v[248:249]
	v_pk_mul_f32 v[120:121], v[120:121], v[248:249]
	v_pk_mul_f32 v[122:123], v[122:123], v[248:249]
	v_pk_mul_f32 v[124:125], v[124:125], v[248:249]
	v_pk_mul_f32 v[126:127], v[126:127], v[248:249]
	v_pk_mul_f32 v[128:129], v[128:129], v[248:249]
	v_cvt_pk_fp8_f32 v208, v98, v102
	v_cvt_pk_fp8_f32 v209, v114, v118
	v_cvt_pk_fp8_f32 v210, v99, v103
	v_cvt_pk_fp8_f32 v211, v115, v119
	v_cvt_pk_fp8_f32 v212, v100, v104
	v_cvt_pk_fp8_f32 v213, v116, v120
	v_cvt_pk_fp8_f32 v214, v101, v105
	v_cvt_pk_fp8_f32 v215, v117, v121
	v_cvt_pk_fp8_f32 v208, v106, v110 op_sel:[0,0,1]
	v_cvt_pk_fp8_f32 v209, v122, v126 op_sel:[0,0,1]
	v_cvt_pk_fp8_f32 v210, v107, v111 op_sel:[0,0,1]
	v_cvt_pk_fp8_f32 v211, v123, v127 op_sel:[0,0,1]
	v_cvt_pk_fp8_f32 v212, v108, v112 op_sel:[0,0,1]
	v_cvt_pk_fp8_f32 v213, v124, v128 op_sel:[0,0,1]
	v_cvt_pk_fp8_f32 v214, v109, v113 op_sel:[0,0,1]
	v_cvt_pk_fp8_f32 v215, v125, v129 op_sel:[0,0,1]
	s_nop 0
	ds_write2_b64 v141, v[208:209], v[210:211] offset1:16
	ds_write2_b64 v141, v[212:213], v[214:215] offset0:32 offset1:48
	global_load_dwordx4 v[66:69], v130, s[0:1] nt
	global_load_dwordx4 v[70:73], v131, s[0:1] nt
	global_load_dwordx4 v[74:77], v132, s[0:1] nt
	global_load_dwordx4 v[78:81], v133, s[0:1] nt
	global_load_dwordx4 v[82:85], v134, s[0:1] nt
	global_load_dwordx4 v[86:89], v135, s[0:1] nt
	global_load_dwordx4 v[90:93], v136, s[0:1] nt
	global_load_dwordx4 v[94:97], v137, s[0:1] nt
	s_add_u32 s0, s0, 0x10000
	s_addc_u32 s1, s1, 0
	s_waitcnt vmcnt(16)
	v_pk_mul_f32 v[2:3], v[2:3], v[248:249]
	v_pk_mul_f32 v[4:5], v[4:5], v[248:249]
	v_pk_mul_f32 v[6:7], v[6:7], v[248:249]
	v_pk_mul_f32 v[8:9], v[8:9], v[248:249]
	v_pk_mul_f32 v[10:11], v[10:11], v[248:249]
	v_pk_mul_f32 v[12:13], v[12:13], v[248:249]
	v_pk_mul_f32 v[14:15], v[14:15], v[248:249]
	v_pk_mul_f32 v[16:17], v[16:17], v[248:249]
	v_pk_mul_f32 v[18:19], v[18:19], v[248:249]
	v_pk_mul_f32 v[20:21], v[20:21], v[248:249]
	v_pk_mul_f32 v[22:23], v[22:23], v[248:249]
	v_pk_mul_f32 v[24:25], v[24:25], v[248:249]
	v_pk_mul_f32 v[26:27], v[26:27], v[248:249]
	v_pk_mul_f32 v[28:29], v[28:29], v[248:249]
	v_pk_mul_f32 v[30:31], v[30:31], v[248:249]
	v_pk_mul_f32 v[32:33], v[32:33], v[248:249]
	v_cvt_pk_fp8_f32 v200, v2, v6
	v_cvt_pk_fp8_f32 v201, v18, v22
	v_cvt_pk_fp8_f32 v202, v3, v7
	v_cvt_pk_fp8_f32 v203, v19, v23
	v_cvt_pk_fp8_f32 v204, v4, v8
	v_cvt_pk_fp8_f32 v205, v20, v24
	v_cvt_pk_fp8_f32 v206, v5, v9
	v_cvt_pk_fp8_f32 v207, v21, v25
	v_cvt_pk_fp8_f32 v200, v10, v14 op_sel:[0,0,1]
	v_cvt_pk_fp8_f32 v201, v26, v30 op_sel:[0,0,1]
	v_cvt_pk_fp8_f32 v202, v11, v15 op_sel:[0,0,1]
	v_cvt_pk_fp8_f32 v203, v27, v31 op_sel:[0,0,1]
	v_cvt_pk_fp8_f32 v204, v12, v16 op_sel:[0,0,1]
	v_cvt_pk_fp8_f32 v205, v28, v32 op_sel:[0,0,1]
	v_cvt_pk_fp8_f32 v206, v13, v17 op_sel:[0,0,1]
	v_cvt_pk_fp8_f32 v207, v29, v33 op_sel:[0,0,1]
	s_nop 0
	ds_write2_b64 v142, v[200:201], v[202:203] offset1:16
	ds_write2_b64 v142, v[204:205], v[206:207] offset0:32 offset1:48
	global_load_dwordx4 v[98:101], v130, s[0:1] nt
	global_load_dwordx4 v[102:105], v131, s[0:1] nt
	global_load_dwordx4 v[106:109], v132, s[0:1] nt
	global_load_dwordx4 v[110:113], v133, s[0:1] nt
	global_load_dwordx4 v[114:117], v134, s[0:1] nt
	global_load_dwordx4 v[118:121], v135, s[0:1] nt
	global_load_dwordx4 v[122:125], v136, s[0:1] nt
	global_load_dwordx4 v[126:129], v137, s[0:1] nt
	s_add_u32 s0, s0, 0x10000
	s_addc_u32 s1, s1, 0
	s_cmp_ge_u32 s7, s24
	s_cbranch_scc1 .Lcvc_nopf
	s_lshr_b32 s19, s7, 10
	s_and_b32 s20, s7, 0x3ff
	s_cmp_eq_u32 s19, 0
	s_cselect_b32 s0, s34, s36
	s_cselect_b32 s1, s35, s37
	s_cmp_eq_u32 s19, 2
	s_cselect_b32 s0, s38, s0
	s_cselect_b32 s1, s39, s1
	s_lshr_b32 s21, s20, 5
	s_lshl_b32 s21, s21, 24
	s_bfe_u32 s22, s20, 0x40001
	s_lshl_b32 s22, s22, 20
	s_add_u32 s21, s21, s22
	s_and_b32 s22, s20, 1
	s_lshl_b32 s22, s22, 12
	s_add_u32 s21, s21, s22
	s_add_u32 s21, s21, s25
	s_add_u32 s0, s0, s21
	s_addc_u32 s1, s1, 0
	s_waitcnt vmcnt(16)
	v_pk_mul_f32 v[34:35], v[34:35], v[248:249]
	v_pk_mul_f32 v[36:37], v[36:37], v[248:249]
	v_pk_mul_f32 v[38:39], v[38:39], v[248:249]
	v_pk_mul_f32 v[40:41], v[40:41], v[248:249]
	v_pk_mul_f32 v[42:43], v[42:43], v[248:249]
	v_pk_mul_f32 v[44:45], v[44:45], v[248:249]
	v_pk_mul_f32 v[46:47], v[46:47], v[248:249]
	v_pk_mul_f32 v[48:49], v[48:49], v[248:249]
	v_pk_mul_f32 v[50:51], v[50:51], v[248:249]
	v_pk_mul_f32 v[52:53], v[52:53], v[248:249]
	v_pk_mul_f32 v[54:55], v[54:55], v[248:249]
	v_pk_mul_f32 v[56:57], v[56:57], v[248:249]
	v_pk_mul_f32 v[58:59], v[58:59], v[248:249]
	v_pk_mul_f32 v[60:61], v[60:61], v[248:249]
	v_pk_mul_f32 v[62:63], v[62:63], v[248:249]
	v_pk_mul_f32 v[64:65], v[64:65], v[248:249]
	v_cvt_pk_fp8_f32 v208, v34, v38
	v_cvt_pk_fp8_f32 v209, v50, v54
	v_cvt_pk_fp8_f32 v210, v35, v39
	v_cvt_pk_fp8_f32 v211, v51, v55
	v_cvt_pk_fp8_f32 v212, v36, v40
	v_cvt_pk_fp8_f32 v213, v52, v56
	v_cvt_pk_fp8_f32 v214, v37, v41
	v_cvt_pk_fp8_f32 v215, v53, v57
	v_cvt_pk_fp8_f32 v208, v42, v46 op_sel:[0,0,1]
	v_cvt_pk_fp8_f32 v209, v58, v62 op_sel:[0,0,1]
	v_cvt_pk_fp8_f32 v210, v43, v47 op_sel:[0,0,1]
	v_cvt_pk_fp8_f32 v211, v59, v63 op_sel:[0,0,1]
	v_cvt_pk_fp8_f32 v212, v44, v48 op_sel:[0,0,1]
	v_cvt_pk_fp8_f32 v213, v60, v64 op_sel:[0,0,1]
	v_cvt_pk_fp8_f32 v214, v45, v49 op_sel:[0,0,1]
	v_cvt_pk_fp8_f32 v215, v61, v65 op_sel:[0,0,1]
	s_nop 0
	ds_write2_b64 v143, v[208:209], v[210:211] offset1:16
	ds_write2_b64 v143, v[212:213], v[214:215] offset0:32 offset1:48
	global_load_dwordx4 v[2:5], v130, s[0:1] nt
	global_load_dwordx4 v[6:9], v131, s[0:1] nt
	global_load_dwordx4 v[10:13], v132, s[0:1] nt
	global_load_dwordx4 v[14:17], v133, s[0:1] nt
	global_load_dwordx4 v[18:21], v134, s[0:1] nt
	global_load_dwordx4 v[22:25], v135, s[0:1] nt
	global_load_dwordx4 v[26:29], v136, s[0:1] nt
	global_load_dwordx4 v[30:33], v137, s[0:1] nt
	s_add_u32 s0, s0, 0x10000
	s_addc_u32 s1, s1, 0
	s_waitcnt vmcnt(16)
	v_pk_mul_f32 v[66:67], v[66:67], v[248:249]
	v_pk_mul_f32 v[68:69], v[68:69], v[248:249]
	v_pk_mul_f32 v[70:71], v[70:71], v[248:249]
	v_pk_mul_f32 v[72:73], v[72:73], v[248:249]
	v_pk_mul_f32 v[74:75], v[74:75], v[248:249]
	v_pk_mul_f32 v[76:77], v[76:77], v[248:249]
	v_pk_mul_f32 v[78:79], v[78:79], v[248:249]
	v_pk_mul_f32 v[80:81], v[80:81], v[248:249]
	v_pk_mul_f32 v[82:83], v[82:83], v[248:249]
	v_pk_mul_f32 v[84:85], v[84:85], v[248:249]
	v_pk_mul_f32 v[86:87], v[86:87], v[248:249]
	v_pk_mul_f32 v[88:89], v[88:89], v[248:249]
	v_pk_mul_f32 v[90:91], v[90:91], v[248:249]
	v_pk_mul_f32 v[92:93], v[92:93], v[248:249]
	v_pk_mul_f32 v[94:95], v[94:95], v[248:249]
	v_pk_mul_f32 v[96:97], v[96:97], v[248:249]
	v_cvt_pk_fp8_f32 v200, v66, v70
	v_cvt_pk_fp8_f32 v201, v82, v86
	v_cvt_pk_fp8_f32 v202, v67, v71
	v_cvt_pk_fp8_f32 v203, v83, v87
	v_cvt_pk_fp8_f32 v204, v68, v72
	v_cvt_pk_fp8_f32 v205, v84, v88
	v_cvt_pk_fp8_f32 v206, v69, v73
	v_cvt_pk_fp8_f32 v207, v85, v89
	v_cvt_pk_fp8_f32 v200, v74, v78 op_sel:[0,0,1]
	v_cvt_pk_fp8_f32 v201, v90, v94 op_sel:[0,0,1]
	v_cvt_pk_fp8_f32 v202, v75, v79 op_sel:[0,0,1]
	v_cvt_pk_fp8_f32 v203, v91, v95 op_sel:[0,0,1]
	v_cvt_pk_fp8_f32 v204, v76, v80 op_sel:[0,0,1]
	v_cvt_pk_fp8_f32 v205, v92, v96 op_sel:[0,0,1]
	v_cvt_pk_fp8_f32 v206, v77, v81 op_sel:[0,0,1]
	v_cvt_pk_fp8_f32 v207, v93, v97 op_sel:[0,0,1]
	s_nop 0
	ds_write2_b64 v144, v[200:201], v[202:203] offset1:16
	ds_write2_b64 v144, v[204:205], v[206:207] offset0:32 offset1:48
	global_load_dwordx4 v[34:37], v130, s[0:1] nt
	global_load_dwordx4 v[38:41], v131, s[0:1] nt
	global_load_dwordx4 v[42:45], v132, s[0:1] nt
	global_load_dwordx4 v[46:49], v133, s[0:1] nt
	global_load_dwordx4 v[50:53], v134, s[0:1] nt
	global_load_dwordx4 v[54:57], v135, s[0:1] nt
	global_load_dwordx4 v[58:61], v136, s[0:1] nt
	global_load_dwordx4 v[62:65], v137, s[0:1] nt
	s_add_u32 s0, s0, 0x10000
	s_addc_u32 s1, s1, 0
	s_waitcnt vmcnt(16)
	v_pk_mul_f32 v[98:99], v[98:99], v[248:249]
	v_pk_mul_f32 v[100:101], v[100:101], v[248:249]
	v_pk_mul_f32 v[102:103], v[102:103], v[248:249]
	v_pk_mul_f32 v[104:105], v[104:105], v[248:249]
	v_pk_mul_f32 v[106:107], v[106:107], v[248:249]
	v_pk_mul_f32 v[108:109], v[108:109], v[248:249]
	v_pk_mul_f32 v[110:111], v[110:111], v[248:249]
	v_pk_mul_f32 v[112:113], v[112:113], v[248:249]
	v_pk_mul_f32 v[114:115], v[114:115], v[248:249]
	v_pk_mul_f32 v[116:117], v[116:117], v[248:249]
	v_pk_mul_f32 v[118:119], v[118:119], v[248:249]
	v_pk_mul_f32 v[120:121], v[120:121], v[248:249]
	v_pk_mul_f32 v[122:123], v[122:123], v[248:249]
	v_pk_mul_f32 v[124:125], v[124:125], v[248:249]
	v_pk_mul_f32 v[126:127], v[126:127], v[248:249]
	v_pk_mul_f32 v[128:129], v[128:129], v[248:249]
	v_cvt_pk_fp8_f32 v208, v98, v102
	v_cvt_pk_fp8_f32 v209, v114, v118
	v_cvt_pk_fp8_f32 v210, v99, v103
	v_cvt_pk_fp8_f32 v211, v115, v119
	v_cvt_pk_fp8_f32 v212, v100, v104
	v_cvt_pk_fp8_f32 v213, v116, v120
	v_cvt_pk_fp8_f32 v214, v101, v105
	v_cvt_pk_fp8_f32 v215, v117, v121
	v_cvt_pk_fp8_f32 v208, v106, v110 op_sel:[0,0,1]
	v_cvt_pk_fp8_f32 v209, v122, v126 op_sel:[0,0,1]
	v_cvt_pk_fp8_f32 v210, v107, v111 op_sel:[0,0,1]
	v_cvt_pk_fp8_f32 v211, v123, v127 op_sel:[0,0,1]
	v_cvt_pk_fp8_f32 v212, v108, v112 op_sel:[0,0,1]
	v_cvt_pk_fp8_f32 v213, v124, v128 op_sel:[0,0,1]
	v_cvt_pk_fp8_f32 v214, v109, v113 op_sel:[0,0,1]
	v_cvt_pk_fp8_f32 v215, v125, v129 op_sel:[0,0,1]
	s_nop 0
	ds_write2_b64 v145, v[208:209], v[210:211] offset1:16
	ds_write2_b64 v145, v[212:213], v[214:215] offset0:32 offset1:48
	global_load_dwordx4 v[66:69], v130, s[0:1] nt
	global_load_dwordx4 v[70:73], v131, s[0:1] nt
	global_load_dwordx4 v[74:77], v132, s[0:1] nt
	global_load_dwordx4 v[78:81], v133, s[0:1] nt
	global_load_dwordx4 v[82:85], v134, s[0:1] nt
	global_load_dwordx4 v[86:89], v135, s[0:1] nt
	global_load_dwordx4 v[90:93], v136, s[0:1] nt
	global_load_dwordx4 v[94:97], v137, s[0:1] nt
	s_add_u32 s0, s0, 0x10000
	s_addc_u32 s1, s1, 0
	s_branch .Lcvc_stores

.Lcvc_stores:
	s_lshr_b32 s19, s6, 10
	s_and_b32 s20, s6, 0x3ff
	s_lshr_b32 s21, s20, 5
	s_bfe_u32 s22, s20, 0x40001
	s_lshl_b32 s22, s22, 7
	s_and_b32 s23, s20, 1
	s_cmp_eq_u32 s19, 2
	s_cbranch_scc1 .Lcvc_ddown
	s_lshl_b32 s21, s21, 23
	s_lshl_b32 s23, s23, 22
	s_lshl_b32 s19, s19, 18
	s_add_u32 s21, s21, s22
	s_add_u32 s21, s21, s23
	s_add_u32 s21, s21, s19
	s_add_u32 s21, s21, 0x2a800000
	s_mov_b32 s28, 0x60000
	s_branch .Lcvc_djoin
.Lcvc_ddown:
	s_lshl_b32 s21, s21, 22
	s_lshl_b32 s23, s23, 21
	s_add_u32 s21, s21, s22
	s_add_u32 s21, s21, s23
	s_add_u32 s21, s21, 0x4a800000
	s_mov_b32 s28, 0x20000
.Lcvc_djoin:
	s_add_u32 s4, s40, s21
	s_addc_u32 s5, s41, 0
	s_waitcnt lgkmcnt(0)
	s_barrier
	ds_read_b128 v[216:219], v146
	ds_read_b128 v[220:223], v146 offset:8192
	ds_read_b128 v[224:227], v146 offset:16384
	ds_read_b128 v[228:231], v146 offset:24576
	s_waitcnt lgkmcnt(3)
	v_cndmask_b32_e64 v232, v216, v218, s[30:31]
	v_cndmask_b32_e64 v233, v217, v219, s[30:31]
	v_cndmask_b32_e64 v234, v218, v216, s[30:31]
	v_cndmask_b32_e64 v235, v219, v217, s[30:31]
	global_store_dwordx4 v148, v[232:235], s[4:5] nt
	s_add_u32 s4, s4, 0x20000
	s_addc_u32 s5, s5, 0
	s_waitcnt lgkmcnt(2)
	v_cndmask_b32_e64 v236, v220, v222, s[30:31]
	v_cndmask_b32_e64 v237, v221, v223, s[30:31]
	v_cndmask_b32_e64 v238, v222, v220, s[30:31]
	v_cndmask_b32_e64 v239, v223, v221, s[30:31]
	global_store_dwordx4 v148, v[236:239], s[4:5] nt
	s_add_u32 s4, s4, s28
	s_addc_u32 s5, s5, 0
	s_waitcnt lgkmcnt(1)
	v_cndmask_b32_e64 v240, v224, v226, s[30:31]
	v_cndmask_b32_e64 v241, v225, v227, s[30:31]
	v_cndmask_b32_e64 v242, v226, v224, s[30:31]
	v_cndmask_b32_e64 v243, v227, v225, s[30:31]
	global_store_dwordx4 v148, v[240:243], s[4:5] nt
	s_add_u32 s4, s4, 0x20000
	s_addc_u32 s5, s5, 0
	s_waitcnt lgkmcnt(0)
	v_cndmask_b32_e64 v244, v228, v230, s[30:31]
	v_cndmask_b32_e64 v245, v229, v231, s[30:31]
	v_cndmask_b32_e64 v246, v230, v228, s[30:31]
	v_cndmask_b32_e64 v247, v231, v229, s[30:31]
	global_store_dwordx4 v148, v[244:247], s[4:5] nt
	s_add_u32 s4, s4, s28
	s_addc_u32 s5, s5, 0
	ds_read_b128 v[216:219], v146 offset:32768
	ds_read_b128 v[220:223], v146 offset:40960
	ds_read_b128 v[224:227], v146 offset:49152
	ds_read_b128 v[228:231], v146 offset:57344
	s_waitcnt lgkmcnt(3)
	v_cndmask_b32_e64 v232, v216, v218, s[30:31]
	v_cndmask_b32_e64 v233, v217, v219, s[30:31]
	v_cndmask_b32_e64 v234, v218, v216, s[30:31]
	v_cndmask_b32_e64 v235, v219, v217, s[30:31]
	global_store_dwordx4 v148, v[232:235], s[4:5] nt
	s_add_u32 s4, s4, 0x20000
	s_addc_u32 s5, s5, 0
	s_waitcnt lgkmcnt(2)
	v_cndmask_b32_e64 v236, v220, v222, s[30:31]
	v_cndmask_b32_e64 v237, v221, v223, s[30:31]
	v_cndmask_b32_e64 v238, v222, v220, s[30:31]
	v_cndmask_b32_e64 v239, v223, v221, s[30:31]
	global_store_dwordx4 v148, v[236:239], s[4:5] nt
	s_add_u32 s4, s4, s28
	s_addc_u32 s5, s5, 0
	s_waitcnt lgkmcnt(1)
	v_cndmask_b32_e64 v240, v224, v226, s[30:31]
	v_cndmask_b32_e64 v241, v225, v227, s[30:31]
	v_cndmask_b32_e64 v242, v226, v224, s[30:31]
	v_cndmask_b32_e64 v243, v227, v225, s[30:31]
	global_store_dwordx4 v148, v[240:243], s[4:5] nt
	s_add_u32 s4, s4, 0x20000
	s_addc_u32 s5, s5, 0
	s_waitcnt lgkmcnt(0)
	v_cndmask_b32_e64 v244, v228, v230, s[30:31]
	v_cndmask_b32_e64 v245, v229, v231, s[30:31]
	v_cndmask_b32_e64 v246, v230, v228, s[30:31]
	v_cndmask_b32_e64 v247, v231, v229, s[30:31]
	global_store_dwordx4 v148, v[244:247], s[4:5] nt
	s_add_u32 s4, s4, s28
	s_addc_u32 s5, s5, 0
	ds_read_b128 v[216:219], v147
	ds_read_b128 v[220:223], v147 offset:8192
	ds_read_b128 v[224:227], v147 offset:16384
	ds_read_b128 v[228:231], v147 offset:24576
	s_waitcnt lgkmcnt(3)
	v_cndmask_b32_e64 v232, v216, v218, s[30:31]
	v_cndmask_b32_e64 v233, v217, v219, s[30:31]
	v_cndmask_b32_e64 v234, v218, v216, s[30:31]
	v_cndmask_b32_e64 v235, v219, v217, s[30:31]
	global_store_dwordx4 v148, v[232:235], s[4:5] nt
	s_add_u32 s4, s4, 0x20000
	s_addc_u32 s5, s5, 0
	s_waitcnt lgkmcnt(2)
	v_cndmask_b32_e64 v236, v220, v222, s[30:31]
	v_cndmask_b32_e64 v237, v221, v223, s[30:31]
	v_cndmask_b32_e64 v238, v222, v220, s[30:31]
	v_cndmask_b32_e64 v239, v223, v221, s[30:31]
	global_store_dwordx4 v148, v[236:239], s[4:5] nt
	s_add_u32 s4, s4, s28
	s_addc_u32 s5, s5, 0
	s_waitcnt lgkmcnt(1)
	v_cndmask_b32_e64 v240, v224, v226, s[30:31]
	v_cndmask_b32_e64 v241, v225, v227, s[30:31]
	v_cndmask_b32_e64 v242, v226, v224, s[30:31]
	v_cndmask_b32_e64 v243, v227, v225, s[30:31]
	global_store_dwordx4 v148, v[240:243], s[4:5] nt
	s_add_u32 s4, s4, 0x20000
	s_addc_u32 s5, s5, 0
	s_waitcnt lgkmcnt(0)
	v_cndmask_b32_e64 v244, v228, v230, s[30:31]
	v_cndmask_b32_e64 v245, v229, v231, s[30:31]
	v_cndmask_b32_e64 v246, v230, v228, s[30:31]
	v_cndmask_b32_e64 v247, v231, v229, s[30:31]
	global_store_dwordx4 v148, v[244:247], s[4:5] nt
	s_add_u32 s4, s4, s28
	s_addc_u32 s5, s5, 0
	ds_read_b128 v[216:219], v147 offset:32768
	ds_read_b128 v[220:223], v147 offset:40960
	ds_read_b128 v[224:227], v147 offset:49152
	ds_read_b128 v[228:231], v147 offset:57344
	s_waitcnt lgkmcnt(3)
	v_cndmask_b32_e64 v232, v216, v218, s[30:31]
	v_cndmask_b32_e64 v233, v217, v219, s[30:31]
	v_cndmask_b32_e64 v234, v218, v216, s[30:31]
	v_cndmask_b32_e64 v235, v219, v217, s[30:31]
	global_store_dwordx4 v148, v[232:235], s[4:5] nt
	s_add_u32 s4, s4, 0x20000
	s_addc_u32 s5, s5, 0
	s_waitcnt lgkmcnt(2)
	v_cndmask_b32_e64 v236, v220, v222, s[30:31]
	v_cndmask_b32_e64 v237, v221, v223, s[30:31]
	v_cndmask_b32_e64 v238, v222, v220, s[30:31]
	v_cndmask_b32_e64 v239, v223, v221, s[30:31]
	global_store_dwordx4 v148, v[236:239], s[4:5] nt
	s_add_u32 s4, s4, s28
	s_addc_u32 s5, s5, 0
	s_waitcnt lgkmcnt(1)
	v_cndmask_b32_e64 v240, v224, v226, s[30:31]
	v_cndmask_b32_e64 v241, v225, v227, s[30:31]
	v_cndmask_b32_e64 v242, v226, v224, s[30:31]
	v_cndmask_b32_e64 v243, v227, v225, s[30:31]
	global_store_dwordx4 v148, v[240:243], s[4:5] nt
	s_add_u32 s4, s4, 0x20000
	s_addc_u32 s5, s5, 0
	s_waitcnt lgkmcnt(0)
	v_cndmask_b32_e64 v244, v228, v230, s[30:31]
	v_cndmask_b32_e64 v245, v229, v231, s[30:31]
	v_cndmask_b32_e64 v246, v230, v228, s[30:31]
	v_cndmask_b32_e64 v247, v231, v229, s[30:31]
	global_store_dwordx4 v148, v[244:247], s[4:5] nt
	s_barrier
	s_mov_b32 s6, s7
	s_mov_b32 s7, s44
	s_mov_b32 s44, s45
	s_mov_b32 s45, 0xffff
	s_cmp_lt_u32 s6, s24
	s_cbranch_scc1 .Lcvc_loop
.Lcvc_done:
	s_waitcnt vmcnt(0) lgkmcnt(0)
	s_barrier
	s_branch .LBB0_877
